# g22: g21 + P0: read-once f32 inputs (w_in tiles, x rows) loaded non-temporal so XN1/WinT stay in the memory-side cache for P1
# speedup vs baseline: 1.0147x; 1.0147x over previous
.LBB0_13:
	s_andn2_b64 vcc, exec, s[10:11]
	s_cbranch_vccnz .LBB0_10
	s_mul_hi_i32 s0, s40, 0x2e8ba2e9
	s_lshr_b32 s10, s0, 31
	s_ashr_i32 s0, s0, 6
	s_add_i32 s0, s0, s10
	s_mul_i32 s10, s0, 0xfffffea0
	s_mul_i32 s11, s0, 0xffffd400
	s_add_i32 s10, s40, s10
	s_add_i32 s12, s16, s11
	s_cmpk_gt_i32 s10, 0x9f
	s_cselect_b32 s10, 32, 0
	s_add_i32 s42, s12, s10
	s_lshl_b32 s10, s0, 7
	v_or_b32_e32 v39, s10, v1
	v_mov_b64_e32 v[40:41], s[68:69]
	v_mad_i64_i32 v[40:41], s[44:45], v39, s23, v[40:41]
	s_ashr_i32 s43, s42, 31
	v_lshl_add_u64 v[40:41], s[42:43], 2, v[40:41]
	v_lshl_add_u64 v[40:41], v[40:41], 0, v[2:3]
	v_add_co_u32_e32 v82, vcc, s28, v40
	s_ashr_i32 s13, s12, 31
	s_nop 0
	v_addc_co_u32_e32 v83, vcc, 0, v41, vcc
	v_add_co_u32_e32 v78, vcc, s24, v40
	s_lshl_b64 s[12:13], s[12:13], 12
	s_nop 0
	v_addc_co_u32_e32 v79, vcc, 0, v41, vcc
	v_add_co_u32_e32 v90, vcc, s20, v40
	global_load_dwordx4 v[74:77], v[40:41], off nt
	s_nop 0
	global_load_dwordx4 v[78:81], v[78:79], off offset:1536 nt
	v_addc_co_u32_e32 v91, vcc, 0, v41, vcc
	v_add_co_u32_e32 v86, vcc, s29, v40
	s_add_u32 s0, s7, s12
	s_nop 0
	v_addc_co_u32_e32 v87, vcc, 0, v41, vcc
	v_add_co_u32_e32 v94, vcc, s25, v40
	global_load_dwordx4 v[82:85], v[82:83], off offset:1024 nt
	s_nop 0
	global_load_dwordx4 v[86:89], v[86:87], off offset:2560 nt
	v_addc_co_u32_e32 v95, vcc, 0, v41, vcc
	v_add_co_u32_e32 v98, vcc, s26, v40
	global_load_dwordx4 v[90:93], v[90:91], off offset:3072 nt
	s_nop 0
	global_load_dwordx4 v[94:97], v[94:95], off offset:512 nt
	v_addc_co_u32_e32 v99, vcc, 0, v41, vcc
	v_add_co_u32_e32 v106, vcc, s30, v40
	s_addc_u32 s12, s9, s13
	s_nop 0
	v_addc_co_u32_e32 v107, vcc, 0, v41, vcc
	v_add_co_u32_e32 v102, vcc, s27, v40
	s_ashr_i32 s11, s10, 31
	s_nop 0
	v_addc_co_u32_e32 v103, vcc, 0, v41, vcc
	v_add_co_u32_e32 v110, vcc, s31, v40
	global_load_dwordx4 v[98:101], v[98:99], off offset:2048 nt
	s_nop 0
	global_load_dwordx4 v[102:105], v[102:103], off offset:3584 nt
	v_addc_co_u32_e32 v111, vcc, 0, v41, vcc
	v_add_co_u32_e32 v114, vcc, s34, v40
	s_lshl_b64 s[10:11], s[10:11], 1
	s_nop 0
	v_addc_co_u32_e32 v115, vcc, 0, v41, vcc
	v_add_co_u32_e32 v118, vcc, s35, v40
	s_add_u32 s10, s0, s10
	s_nop 0
	v_addc_co_u32_e32 v119, vcc, 0, v41, vcc
	v_add_co_u32_e32 v122, vcc, s36, v40
	global_load_dwordx4 v[106:109], v[106:107], off nt
	s_nop 0
	global_load_dwordx4 v[110:113], v[110:111], off offset:1536 nt
	s_nop 0
	global_load_dwordx4 v[114:117], v[114:115], off offset:3072 nt
	s_nop 0
	global_load_dwordx4 v[118:121], v[118:119], off offset:512 nt
	v_addc_co_u32_e32 v123, vcc, 0, v41, vcc
	v_add_co_u32_e32 v126, vcc, s37, v40
	s_addc_u32 s11, s12, s11
	s_nop 0
	v_addc_co_u32_e32 v127, vcc, 0, v41, vcc
	global_load_dwordx4 v[122:125], v[122:123], off offset:2048 nt
	s_nop 0
	global_load_dwordx4 v[126:129], v[126:127], off offset:3584 nt
	v_add_co_u32_e32 v130, vcc, s38, v40
	v_mov_b32_e32 v39, v3
	s_nop 0
	v_addc_co_u32_e32 v131, vcc, 0, v41, vcc
	global_load_dwordx4 v[130:133], v[130:131], off offset:1024 nt
	v_add_co_u32_e32 v40, vcc, s39, v40
	v_lshl_add_u64 v[38:39], s[10:11], 0, v[38:39]
	s_nop 0
	v_addc_co_u32_e32 v41, vcc, 0, v41, vcc
	global_load_dwordx4 v[134:137], v[40:41], off offset:2560 nt
	s_waitcnt vmcnt(13)
	ds_write2_b32 v72, v82, v83 offset1:1
	ds_write2_b32 v73, v84, v85 offset1:1
	ds_write2_b32 v42, v74, v75 offset1:1
	ds_write2_b32 v42, v76, v77 offset0:2 offset1:3
	ds_write2_b32 v43, v78, v79 offset1:1
	ds_write2_b32 v44, v80, v81 offset1:1
	s_waitcnt vmcnt(11)
	ds_write2_b32 v45, v90, v91 offset1:1
	ds_write2_b32 v46, v92, v93 offset1:1
	s_waitcnt vmcnt(10)
	ds_write2_b32 v47, v94, v95 offset1:1
	ds_write2_b32 v48, v96, v97 offset1:1
	s_waitcnt vmcnt(9)
	ds_write2_b32 v49, v98, v99 offset1:1
	ds_write2_b32 v50, v100, v101 offset1:1
	ds_write2_b32 v68, v86, v87 offset1:1
	ds_write2_b32 v69, v88, v89 offset1:1
	s_waitcnt vmcnt(7)
	ds_write2_b32 v70, v106, v107 offset1:1
	ds_write2_b32 v71, v108, v109 offset1:1
	ds_write2_b32 v51, v102, v103 offset1:1
	ds_write2_b32 v52, v104, v105 offset1:1
	s_waitcnt vmcnt(6)
	ds_write2_b32 v54, v110, v111 offset1:1
	ds_write2_b32 v55, v112, v113 offset1:1
	s_waitcnt vmcnt(5)
	ds_write2_b32 v56, v114, v115 offset1:1
	ds_write2_b32 v57, v116, v117 offset1:1
	s_waitcnt vmcnt(4)
	ds_write2_b32 v58, v118, v119 offset1:1
	ds_write2_b32 v59, v120, v121 offset1:1
	s_waitcnt vmcnt(3)
	ds_write2_b32 v60, v122, v123 offset1:1
	ds_write2_b32 v61, v124, v125 offset1:1
	s_waitcnt vmcnt(2)
	ds_write2_b32 v62, v126, v127 offset1:1
	ds_write2_b32 v63, v128, v129 offset1:1
	s_waitcnt vmcnt(1)
	ds_write2_b32 v64, v130, v131 offset1:1
	ds_write2_b32 v65, v132, v133 offset1:1
	s_waitcnt vmcnt(0)
	ds_write2_b32 v66, v134, v135 offset1:1
	ds_write2_b32 v67, v136, v137 offset1:1
	s_waitcnt lgkmcnt(0)
	ds_read2_b32 v[40:41], v5 offset1:4
	ds_read2_b32 v[58:59], v5 offset0:33 offset1:37
	ds_read2_b32 v[60:61], v5 offset0:66 offset1:70
	ds_read2_b32 v[62:63], v5 offset0:99 offset1:103
	ds_read2_b32 v[64:65], v5 offset0:132 offset1:136
	s_waitcnt lgkmcnt(4)
	v_bfe_u32 v54, v40, 16, 1
	v_add3_u32 v40, v40, v54, s21
	s_waitcnt lgkmcnt(3)
	v_bfe_u32 v54, v58, 16, 1
	v_lshrrev_b32_e32 v40, 16, v40
	v_add3_u32 v54, v58, v54, s21
	ds_read2_b32 v[66:67], v5 offset0:165 offset1:169
	v_and_or_b32 v54, v54, s22, v40
	s_waitcnt lgkmcnt(3)
	v_bfe_u32 v40, v60, 16, 1
	v_add3_u32 v40, v60, v40, s21
	s_waitcnt lgkmcnt(2)
	v_bfe_u32 v55, v62, 16, 1
	ds_read2_b32 v[68:69], v5 offset0:198 offset1:202
	v_lshrrev_b32_e32 v40, 16, v40
	v_add3_u32 v55, v62, v55, s21
	ds_read2_b32 v[70:71], v5 offset0:231 offset1:235
	v_and_or_b32 v55, v55, s22, v40
	s_waitcnt lgkmcnt(3)
	v_bfe_u32 v40, v64, 16, 1
	v_add3_u32 v40, v64, v40, s21
	s_waitcnt lgkmcnt(2)
	v_bfe_u32 v56, v66, 16, 1
	v_lshrrev_b32_e32 v40, 16, v40
	v_add3_u32 v56, v66, v56, s21
	v_and_or_b32 v56, v56, s22, v40
	s_waitcnt lgkmcnt(1)
	v_bfe_u32 v40, v68, 16, 1
	v_add3_u32 v40, v68, v40, s21
	s_waitcnt lgkmcnt(0)
	v_bfe_u32 v57, v70, 16, 1
	v_lshrrev_b32_e32 v40, 16, v40
	v_add3_u32 v57, v70, v57, s21
	v_and_or_b32 v57, v57, s22, v40
	v_bfe_u32 v40, v41, 16, 1
	v_add3_u32 v40, v41, v40, s21
	v_bfe_u32 v41, v59, 16, 1
	v_lshl_add_u64 v[72:73], v[38:39], 0, v[22:23]
	v_lshrrev_b32_e32 v40, 16, v40
	v_add3_u32 v41, v59, v41, s21
	global_store_dwordx4 v[72:73], v[54:57], off
	v_lshl_add_u64 v[72:73], v[38:39], 0, v[26:27]
	s_nop 0
	v_and_or_b32 v54, v41, s22, v40
	v_bfe_u32 v40, v61, 16, 1
	v_add3_u32 v40, v61, v40, s21
	v_bfe_u32 v41, v63, 16, 1
	v_lshrrev_b32_e32 v40, 16, v40
	v_add3_u32 v41, v63, v41, s21
	v_and_or_b32 v55, v41, s22, v40
	v_bfe_u32 v40, v65, 16, 1
	v_add3_u32 v40, v65, v40, s21
	v_bfe_u32 v41, v67, 16, 1
	v_lshrrev_b32_e32 v40, 16, v40
	v_add3_u32 v41, v67, v41, s21
	v_and_or_b32 v56, v41, s22, v40
	v_bfe_u32 v40, v69, 16, 1
	v_add3_u32 v40, v69, v40, s21
	v_lshrrev_b32_e32 v57, 16, v40
	v_bfe_u32 v40, v71, 16, 1
	v_add3_u32 v58, v71, v40, s21
	ds_read2_b32 v[40:41], v5 offset0:8 offset1:12
	v_and_or_b32 v57, v58, s22, v57
	v_lshl_add_u64 v[58:59], v[38:39], 0, v[24:25]
	global_store_dwordx4 v[58:59], v[54:57], off
	ds_read2_b32 v[58:59], v5 offset0:41 offset1:45
	ds_read2_b32 v[60:61], v5 offset0:74 offset1:78
	ds_read2_b32 v[62:63], v5 offset0:107 offset1:111
	s_waitcnt lgkmcnt(3)
	v_bfe_u32 v54, v40, 16, 1
	v_add3_u32 v40, v40, v54, s21
	s_waitcnt lgkmcnt(2)
	v_bfe_u32 v54, v58, 16, 1
	ds_read2_b32 v[64:65], v5 offset0:140 offset1:144
	v_lshrrev_b32_e32 v40, 16, v40
	v_add3_u32 v54, v58, v54, s21
	ds_read2_b32 v[66:67], v5 offset0:173 offset1:177
	v_and_or_b32 v54, v54, s22, v40
	s_waitcnt lgkmcnt(3)
	v_bfe_u32 v40, v60, 16, 1
	v_add3_u32 v40, v60, v40, s21
	s_waitcnt lgkmcnt(2)
	v_bfe_u32 v55, v62, 16, 1
	ds_read2_b32 v[68:69], v5 offset0:206 offset1:210
	v_lshrrev_b32_e32 v40, 16, v40
	v_add3_u32 v55, v62, v55, s21
	ds_read2_b32 v[70:71], v5 offset0:239 offset1:243
	v_and_or_b32 v55, v55, s22, v40
	s_waitcnt lgkmcnt(3)
	v_bfe_u32 v40, v64, 16, 1
	v_add3_u32 v40, v64, v40, s21
	s_waitcnt lgkmcnt(2)
	v_bfe_u32 v56, v66, 16, 1
	v_lshrrev_b32_e32 v40, 16, v40
	v_add3_u32 v56, v66, v56, s21
	v_and_or_b32 v56, v56, s22, v40
	s_waitcnt lgkmcnt(1)
	v_bfe_u32 v40, v68, 16, 1
	v_add3_u32 v40, v68, v40, s21
	s_waitcnt lgkmcnt(0)
	v_bfe_u32 v57, v70, 16, 1
	v_lshrrev_b32_e32 v40, 16, v40
	v_add3_u32 v57, v70, v57, s21
	v_and_or_b32 v57, v57, s22, v40
	v_bfe_u32 v40, v41, 16, 1
	v_add3_u32 v40, v41, v40, s21
	v_bfe_u32 v41, v59, 16, 1
	v_lshrrev_b32_e32 v40, 16, v40
	v_add3_u32 v41, v59, v41, s21
	global_store_dwordx4 v[72:73], v[54:57], off
	v_lshl_add_u64 v[72:73], v[38:39], 0, v[30:31]
	s_nop 0
	v_and_or_b32 v54, v41, s22, v40
	v_bfe_u32 v40, v61, 16, 1
	v_add3_u32 v40, v61, v40, s21
	v_bfe_u32 v41, v63, 16, 1
	v_lshrrev_b32_e32 v40, 16, v40
	v_add3_u32 v41, v63, v41, s21
	v_and_or_b32 v55, v41, s22, v40
	v_bfe_u32 v40, v65, 16, 1
	v_add3_u32 v40, v65, v40, s21
	v_bfe_u32 v41, v67, 16, 1
	v_lshrrev_b32_e32 v40, 16, v40
	v_add3_u32 v41, v67, v41, s21
	v_and_or_b32 v56, v41, s22, v40
	v_bfe_u32 v40, v69, 16, 1
	v_add3_u32 v40, v69, v40, s21
	v_lshrrev_b32_e32 v57, 16, v40
	v_bfe_u32 v40, v71, 16, 1
	v_add3_u32 v58, v71, v40, s21
	ds_read2_b32 v[40:41], v5 offset0:16 offset1:20
	v_and_or_b32 v57, v58, s22, v57
	v_lshl_add_u64 v[58:59], v[38:39], 0, v[28:29]
	global_store_dwordx4 v[58:59], v[54:57], off
	ds_read2_b32 v[58:59], v5 offset0:49 offset1:53
	ds_read2_b32 v[60:61], v5 offset0:82 offset1:86
	ds_read2_b32 v[62:63], v5 offset0:115 offset1:119
	s_waitcnt lgkmcnt(3)
	v_bfe_u32 v54, v40, 16, 1
	v_add3_u32 v40, v40, v54, s21
	s_waitcnt lgkmcnt(2)
	v_bfe_u32 v54, v58, 16, 1
	ds_read2_b32 v[64:65], v5 offset0:148 offset1:152
	v_lshrrev_b32_e32 v40, 16, v40
	v_add3_u32 v54, v58, v54, s21
	ds_read2_b32 v[66:67], v5 offset0:181 offset1:185
	v_and_or_b32 v54, v54, s22, v40
	s_waitcnt lgkmcnt(3)
	v_bfe_u32 v40, v60, 16, 1
	v_add3_u32 v40, v60, v40, s21
	s_waitcnt lgkmcnt(2)
	v_bfe_u32 v55, v62, 16, 1
	ds_read2_b32 v[68:69], v5 offset0:214 offset1:218
	v_lshrrev_b32_e32 v40, 16, v40
	v_add3_u32 v55, v62, v55, s21
	ds_read2_b32 v[70:71], v5 offset0:247 offset1:251
	v_and_or_b32 v55, v55, s22, v40
	s_waitcnt lgkmcnt(3)
	v_bfe_u32 v40, v64, 16, 1
	v_add3_u32 v40, v64, v40, s21
	s_waitcnt lgkmcnt(2)
	v_bfe_u32 v56, v66, 16, 1
	v_lshrrev_b32_e32 v40, 16, v40
	v_add3_u32 v56, v66, v56, s21
	v_and_or_b32 v56, v56, s22, v40
	s_waitcnt lgkmcnt(1)
	v_bfe_u32 v40, v68, 16, 1
	v_add3_u32 v40, v68, v40, s21
	s_waitcnt lgkmcnt(0)
	v_bfe_u32 v57, v70, 16, 1
	v_lshrrev_b32_e32 v40, 16, v40
	v_add3_u32 v57, v70, v57, s21
	v_and_or_b32 v57, v57, s22, v40
	v_bfe_u32 v40, v41, 16, 1
	v_add3_u32 v40, v41, v40, s21
	v_bfe_u32 v41, v59, 16, 1
	v_lshrrev_b32_e32 v40, 16, v40
	v_add3_u32 v41, v59, v41, s21
	global_store_dwordx4 v[72:73], v[54:57], off
	v_lshl_add_u64 v[72:73], v[38:39], 0, v[34:35]
	s_nop 0
	v_and_or_b32 v54, v41, s22, v40
	v_bfe_u32 v40, v61, 16, 1
	v_add3_u32 v40, v61, v40, s21
	v_bfe_u32 v41, v63, 16, 1
	v_lshrrev_b32_e32 v40, 16, v40
	v_add3_u32 v41, v63, v41, s21
	v_and_or_b32 v55, v41, s22, v40
	v_bfe_u32 v40, v65, 16, 1
	v_add3_u32 v40, v65, v40, s21
	v_bfe_u32 v41, v67, 16, 1
	v_lshrrev_b32_e32 v40, 16, v40
	v_add3_u32 v41, v67, v41, s21
	v_and_or_b32 v56, v41, s22, v40
	v_bfe_u32 v40, v69, 16, 1
	v_add3_u32 v40, v69, v40, s21
	v_lshrrev_b32_e32 v57, 16, v40
	v_bfe_u32 v40, v71, 16, 1
	v_add3_u32 v58, v71, v40, s21
	ds_read2_b32 v[40:41], v5 offset0:24 offset1:28
	v_and_or_b32 v57, v58, s22, v57
	v_lshl_add_u64 v[58:59], v[38:39], 0, v[32:33]
	global_store_dwordx4 v[58:59], v[54:57], off
	ds_read2_b32 v[58:59], v5 offset0:57 offset1:61
	ds_read2_b32 v[60:61], v5 offset0:90 offset1:94
	ds_read2_b32 v[62:63], v5 offset0:123 offset1:127
	s_waitcnt lgkmcnt(3)
	v_bfe_u32 v54, v40, 16, 1
	v_add3_u32 v40, v40, v54, s21
	s_waitcnt lgkmcnt(2)
	v_bfe_u32 v54, v58, 16, 1
	ds_read2_b32 v[64:65], v5 offset0:156 offset1:160
	v_lshrrev_b32_e32 v40, 16, v40
	v_add3_u32 v54, v58, v54, s21
	ds_read2_b32 v[66:67], v5 offset0:189 offset1:193
	v_and_or_b32 v54, v54, s22, v40
	s_waitcnt lgkmcnt(3)
	v_bfe_u32 v40, v60, 16, 1
	v_add3_u32 v40, v60, v40, s21
	s_waitcnt lgkmcnt(2)
	v_bfe_u32 v55, v62, 16, 1
	ds_read2_b32 v[68:69], v5 offset0:222 offset1:226
	v_lshrrev_b32_e32 v40, 16, v40
	v_add3_u32 v55, v62, v55, s21
	ds_read2_b32 v[70:71], v53 offset0:127 offset1:131
	v_and_or_b32 v55, v55, s22, v40
	s_waitcnt lgkmcnt(3)
	v_bfe_u32 v40, v64, 16, 1
	v_add3_u32 v40, v64, v40, s21
	s_waitcnt lgkmcnt(2)
	v_bfe_u32 v56, v66, 16, 1
	v_lshrrev_b32_e32 v40, 16, v40
	v_add3_u32 v56, v66, v56, s21
	v_and_or_b32 v56, v56, s22, v40
	s_waitcnt lgkmcnt(1)
	v_bfe_u32 v40, v68, 16, 1
	v_add3_u32 v40, v68, v40, s21
	s_waitcnt lgkmcnt(0)
	v_bfe_u32 v53, v70, 16, 1
	v_lshrrev_b32_e32 v40, 16, v40
	v_add3_u32 v53, v70, v53, s21
	v_and_or_b32 v57, v53, s22, v40
	v_bfe_u32 v40, v41, 16, 1
	v_add3_u32 v40, v41, v40, s21
	v_bfe_u32 v41, v59, 16, 1
	v_lshrrev_b32_e32 v40, 16, v40
	v_add3_u32 v41, v59, v41, s21
	global_store_dwordx4 v[72:73], v[54:57], off
	v_lshl_add_u64 v[38:39], v[38:39], 0, v[36:37]
	s_nop 0
	v_and_or_b32 v54, v41, s22, v40
	v_bfe_u32 v40, v61, 16, 1
	v_add3_u32 v40, v61, v40, s21
	v_bfe_u32 v41, v63, 16, 1
	v_lshrrev_b32_e32 v40, 16, v40
	v_add3_u32 v41, v63, v41, s21
	v_and_or_b32 v55, v41, s22, v40
	v_bfe_u32 v40, v65, 16, 1
	v_add3_u32 v40, v65, v40, s21
	v_bfe_u32 v41, v67, 16, 1
	v_lshrrev_b32_e32 v40, 16, v40
	v_add3_u32 v41, v67, v41, s21
	v_and_or_b32 v56, v41, s22, v40
	v_bfe_u32 v40, v69, 16, 1
	v_add3_u32 v40, v69, v40, s21
	v_bfe_u32 v41, v71, 16, 1
	v_lshrrev_b32_e32 v40, 16, v40
	v_add3_u32 v41, v71, v41, s21
	v_and_or_b32 v57, v41, s22, v40
	global_store_dwordx4 v[38:39], v[54:57], off
	s_waitcnt lgkmcnt(0)
	s_branch .LBB0_10

.LBB0_25:
	global_load_dwordx4 v[30:33], v[44:45], off offset:-4096 nt
	global_load_dwordx4 v[26:29], v[44:45], off offset:-3072 nt
	global_load_dwordx4 v[22:25], v[44:45], off offset:-2048 nt
	global_load_dwordx4 v[14:17], v[44:45], off nt
	global_load_dwordx4 v[18:21], v[44:45], off offset:-1024 nt
	global_load_dwordx4 v[10:13], v[44:45], off offset:1024 nt
	global_load_dwordx4 v[2:5], v[44:45], off offset:3072 nt
	global_load_dwordx4 v[6:9], v[44:45], off offset:2048 nt
	global_load_dwordx4 v[56:59], v[34:35], off
	s_add_i32 s6, s6, s8
	v_lshl_add_u64 v[44:45], v[44:45], 0, s[10:11]
	s_cmpk_lt_i32 s6, 0x4000
	s_waitcnt vmcnt(8)
	v_mov_b32_e32 v62, v31
	s_waitcnt vmcnt(7)
	v_mov_b32_e32 v63, v27
	v_mov_b32_e32 v66, v33
	v_mov_b32_e32 v67, v29
	v_mov_b32_e32 v60, v30
	v_mov_b32_e32 v61, v26
	v_mov_b32_e32 v64, v32
	v_mov_b32_e32 v65, v28
	s_waitcnt vmcnt(6)
	v_pk_mul_f32 v[68:69], v[24:25], v[24:25]
	v_pk_mul_f32 v[70:71], v[22:23], v[22:23]
	v_mov_b32_e32 v84, v30
	v_mov_b32_e32 v85, v32
	s_waitcnt vmcnt(0)
	v_mov_b32_e32 v86, v56
	v_mov_b32_e32 v87, v58
	v_mov_b32_e32 v32, v31
	v_mov_b32_e32 v58, v57
	v_mov_b32_e32 v30, v26
	v_mov_b32_e32 v31, v28
	v_mov_b32_e32 v28, v27
	v_pk_mul_f32 v[26:27], v[62:63], v[62:63]
	v_pk_mul_f32 v[56:57], v[66:67], v[66:67]
	v_pk_mov_b32 v[62:63], v[70:71], v[68:69] op_sel:[1,0]
	v_mov_b32_e32 v71, v69
	v_pk_fma_f32 v[26:27], v[60:61], v[60:61], v[26:27]
	v_pk_fma_f32 v[56:57], v[64:65], v[64:65], v[56:57]
	v_mul_f32_e32 v72, v19, v19
	v_mul_f32_e32 v74, v21, v21
	v_pk_add_f32 v[60:61], v[62:63], v[70:71]
	v_pk_add_f32 v[26:27], v[26:27], v[56:57]
	v_mul_f32_e32 v81, v14, v14
	v_mul_f32_e32 v83, v15, v15
	v_mul_f32_e32 v88, v16, v16
	v_mul_f32_e32 v89, v17, v17
	v_pk_fma_f32 v[66:67], v[18:19], v[18:19], v[72:73] op_sel_hi:[1,1,0]
	v_pk_fma_f32 v[68:69], v[20:21], v[20:21], v[74:75] op_sel_hi:[1,1,0]
	v_pk_add_f32 v[56:57], v[60:61], v[60:61] op_sel:[0,1] op_sel_hi:[1,0]
	v_pk_add_f32 v[26:27], v[26:27], v[26:27] op_sel:[0,1] op_sel_hi:[1,0]
	v_pk_mul_f32 v[76:77], v[12:13], v[12:13]
	v_pk_mul_f32 v[78:79], v[10:11], v[10:11]
	v_mov_b32_e32 v67, v88
	v_mov_b32_e32 v69, v89
	v_mov_b32_e32 v57, v83
	v_mov_b32_e32 v27, v81
	v_pk_mov_b32 v[72:73], v[78:79], v[76:77] op_sel:[1,0]
	v_mov_b32_e32 v79, v77
	v_pk_add_f32 v[60:61], v[66:67], v[68:69]
	v_pk_add_f32 v[26:27], v[26:27], v[56:57]
	v_mul_f32_e32 v80, v7, v7
	v_mul_f32_e32 v82, v9, v9
	v_pk_add_f32 v[62:63], v[72:73], v[78:79]
	v_pk_add_f32 v[26:27], v[26:27], v[60:61]
	v_mul_f32_e32 v90, v2, v2
	v_mul_f32_e32 v91, v3, v3
	v_mul_f32_e32 v92, v4, v4
	v_mul_f32_e32 v93, v5, v5
	v_pk_fma_f32 v[74:75], v[6:7], v[6:7], v[80:81] op_sel_hi:[1,1,0]
	v_pk_fma_f32 v[76:77], v[8:9], v[8:9], v[82:83] op_sel_hi:[1,1,0]
	v_pk_add_f32 v[62:63], v[62:63], v[62:63] op_sel:[0,1] op_sel_hi:[1,0]
	v_pk_add_f32 v[26:27], v[26:27], v[26:27] op_sel:[0,1] op_sel_hi:[1,0]
	v_mov_b32_e32 v75, v92
	v_mov_b32_e32 v77, v93
	v_mov_b32_e32 v63, v91
	v_mov_b32_e32 v27, v90
	v_pk_add_f32 v[64:65], v[74:75], v[76:77]
	v_pk_add_f32 v[26:27], v[26:27], v[62:63]
	s_nop 0
	v_pk_add_f32 v[26:27], v[26:27], v[64:65]
	s_nop 0
	v_add_f32_e32 v26, v26, v27
	ds_bpermute_b32 v27, v1, v26
	s_waitcnt lgkmcnt(0)
	v_add_f32_e32 v26, v26, v27
	ds_bpermute_b32 v27, v48, v26
	s_waitcnt lgkmcnt(0)
	v_add_f32_e32 v26, v26, v27
	ds_bpermute_b32 v27, v49, v26
	s_waitcnt lgkmcnt(0)
	v_add_f32_e32 v26, v26, v27
	ds_bpermute_b32 v27, v50, v26
	s_waitcnt lgkmcnt(0)
	v_add_f32_e32 v26, v26, v27
	ds_bpermute_b32 v27, v51, v26
	s_waitcnt lgkmcnt(0)
	v_add_f32_e32 v26, v26, v27
	ds_bpermute_b32 v27, v52, v26
	s_waitcnt lgkmcnt(0)
	v_add_f32_e32 v26, v26, v27
	v_fmamk_f32 v26, v26, 0x3a000000, v53
	v_mul_f32_e32 v27, 0x4f800000, v26
	v_cmp_gt_f32_e32 vcc, s7, v26
	s_nop 1
	v_cndmask_b32_e32 v26, v26, v27, vcc
	v_sqrt_f32_e32 v27, v26
	s_nop 0
	v_add_u32_e32 v56, -1, v27
	v_add_u32_e32 v57, 1, v27
	v_fma_f32 v60, -v56, v27, v26
	v_fma_f32 v61, -v57, v27, v26
	v_cmp_ge_f32_e64 s[0:1], 0, v60
	s_nop 1
	v_cndmask_b32_e64 v27, v27, v56, s[0:1]
	v_cmp_lt_f32_e64 s[0:1], 0, v61
	s_nop 1
	v_cndmask_b32_e64 v27, v27, v57, s[0:1]
	v_mul_f32_e32 v56, 0x37800000, v27
	v_cndmask_b32_e32 v27, v27, v56, vcc
	v_cmp_class_f32_e32 vcc, v26, v54
	s_nop 1
	v_cndmask_b32_e32 v26, v27, v26, vcc
	v_div_scale_f32 v27, s[0:1], v26, v26, 1.0
	v_rcp_f32_e32 v57, v27
	v_div_scale_f32 v56, vcc, 1.0, v26, 1.0
	v_fma_f32 v60, -v27, v57, 1.0
	v_fmac_f32_e32 v57, v60, v57
	v_mul_f32_e32 v60, v56, v57
	v_fma_f32 v61, -v27, v60, v56
	v_fmac_f32_e32 v60, v61, v57
	v_fma_f32 v27, -v27, v60, v56
	v_div_fmas_f32 v27, v27, v57, v60
	v_div_fixup_f32 v26, v27, v26, 1.0
	v_pk_mul_f32 v[56:57], v[84:85], v[26:27] op_sel_hi:[1,0]
	v_pk_mul_f32 v[32:33], v[32:33], v[26:27] op_sel_hi:[1,0]
	v_pk_mul_f32 v[60:61], v[30:31], v[26:27] op_sel_hi:[1,0]
	v_pk_mul_f32 v[30:31], v[86:87], v[56:57]
	v_pk_mul_f32 v[32:33], v[58:59], v[32:33]
	v_and_b32_sdwa v27, v31, v55 dst_sel:DWORD dst_unused:UNUSED_PAD src0_sel:WORD_1 src1_sel:DWORD
	v_and_b32_sdwa v57, v33, v55 dst_sel:DWORD dst_unused:UNUSED_PAD src0_sel:WORD_1 src1_sel:DWORD
	v_and_b32_sdwa v58, v32, v55 dst_sel:DWORD dst_unused:UNUSED_PAD src0_sel:WORD_1 src1_sel:DWORD
	v_and_b32_sdwa v56, v30, v55 dst_sel:DWORD dst_unused:UNUSED_PAD src0_sel:WORD_1 src1_sel:DWORD
	v_add3_u32 v27, v31, v27, s9
	v_add3_u32 v31, v33, v57, s9
	v_add3_u32 v32, v32, v58, s9
	v_add3_u32 v30, v30, v56, s9
	v_and_b32_e32 v31, 0xffff0000, v31
	v_and_b32_e32 v32, 0xffff0000, v32
	v_or_b32_sdwa v31, v31, v27 dst_sel:DWORD dst_unused:UNUSED_PAD src0_sel:DWORD src1_sel:WORD_1
	v_or_b32_sdwa v30, v32, v30 dst_sel:DWORD dst_unused:UNUSED_PAD src0_sel:DWORD src1_sel:WORD_1
	global_store_dwordx2 v[46:47], v[30:31], off
	global_load_dwordx4 v[30:33], v[34:35], off offset:1024
	v_pk_mul_f32 v[28:29], v[28:29], v[26:27] op_sel_hi:[1,0]
	s_waitcnt vmcnt(0)
	v_mov_b32_e32 v57, v32
	v_mov_b32_e32 v32, v31
	v_mov_b32_e32 v56, v30
	v_pk_mul_f32 v[28:29], v[32:33], v[28:29]
	v_pk_mul_f32 v[30:31], v[56:57], v[60:61]
	v_and_b32_sdwa v33, v29, v55 dst_sel:DWORD dst_unused:UNUSED_PAD src0_sel:WORD_1 src1_sel:DWORD
	v_and_b32_sdwa v56, v28, v55 dst_sel:DWORD dst_unused:UNUSED_PAD src0_sel:WORD_1 src1_sel:DWORD
	v_and_b32_sdwa v27, v31, v55 dst_sel:DWORD dst_unused:UNUSED_PAD src0_sel:WORD_1 src1_sel:DWORD
	v_and_b32_sdwa v32, v30, v55 dst_sel:DWORD dst_unused:UNUSED_PAD src0_sel:WORD_1 src1_sel:DWORD
	v_add3_u32 v29, v29, v33, s9
	v_add3_u32 v28, v28, v56, s9
	v_add3_u32 v30, v30, v32, s9
	v_add3_u32 v27, v31, v27, s9
	v_and_b32_e32 v29, 0xffff0000, v29
	v_and_b32_e32 v28, 0xffff0000, v28
	v_or_b32_sdwa v29, v29, v27 dst_sel:DWORD dst_unused:UNUSED_PAD src0_sel:DWORD src1_sel:WORD_1
	v_or_b32_sdwa v28, v28, v30 dst_sel:DWORD dst_unused:UNUSED_PAD src0_sel:DWORD src1_sel:WORD_1
	global_store_dwordx2 v[46:47], v[28:29], off offset:512
	global_load_dwordx4 v[28:31], v[34:35], off offset:2048
	v_mov_b32_e32 v32, v22
	v_mov_b32_e32 v33, v24
	v_mov_b32_e32 v24, v23
	v_pk_mul_f32 v[22:23], v[32:33], v[26:27] op_sel_hi:[1,0]
	v_pk_mul_f32 v[24:25], v[24:25], v[26:27] op_sel_hi:[1,0]
	s_waitcnt vmcnt(0)
	v_mov_b32_e32 v33, v30
	v_mov_b32_e32 v30, v29
	v_mov_b32_e32 v32, v28
	v_pk_mul_f32 v[24:25], v[30:31], v[24:25]
	v_pk_mul_f32 v[22:23], v[32:33], v[22:23]
	v_and_b32_sdwa v29, v25, v55 dst_sel:DWORD dst_unused:UNUSED_PAD src0_sel:WORD_1 src1_sel:DWORD
	v_and_b32_sdwa v30, v24, v55 dst_sel:DWORD dst_unused:UNUSED_PAD src0_sel:WORD_1 src1_sel:DWORD
	v_and_b32_sdwa v27, v23, v55 dst_sel:DWORD dst_unused:UNUSED_PAD src0_sel:WORD_1 src1_sel:DWORD
	v_and_b32_sdwa v28, v22, v55 dst_sel:DWORD dst_unused:UNUSED_PAD src0_sel:WORD_1 src1_sel:DWORD
	v_add3_u32 v25, v25, v29, s9
	v_add3_u32 v24, v24, v30, s9
	v_add3_u32 v22, v22, v28, s9
	v_add3_u32 v23, v23, v27, s9
	v_and_b32_e32 v25, 0xffff0000, v25
	v_and_b32_e32 v24, 0xffff0000, v24
	v_or_b32_sdwa v23, v25, v23 dst_sel:DWORD dst_unused:UNUSED_PAD src0_sel:DWORD src1_sel:WORD_1
	v_or_b32_sdwa v22, v24, v22 dst_sel:DWORD dst_unused:UNUSED_PAD src0_sel:DWORD src1_sel:WORD_1
	global_store_dwordx2 v[46:47], v[22:23], off offset:1024
	global_load_dwordx4 v[22:25], v[34:35], off offset:3072
	v_mov_b32_e32 v28, v18
	v_mov_b32_e32 v29, v20
	v_mov_b32_e32 v20, v19
	v_pk_mul_f32 v[18:19], v[28:29], v[26:27] op_sel_hi:[1,0]
	v_pk_mul_f32 v[20:21], v[20:21], v[26:27] op_sel_hi:[1,0]
	s_waitcnt vmcnt(0)
	v_mov_b32_e32 v29, v24
	v_mov_b32_e32 v24, v23
	v_mov_b32_e32 v28, v22
	v_pk_mul_f32 v[20:21], v[24:25], v[20:21]
	v_pk_mul_f32 v[18:19], v[28:29], v[18:19]
	v_and_b32_sdwa v24, v21, v55 dst_sel:DWORD dst_unused:UNUSED_PAD src0_sel:WORD_1 src1_sel:DWORD
	v_and_b32_sdwa v25, v20, v55 dst_sel:DWORD dst_unused:UNUSED_PAD src0_sel:WORD_1 src1_sel:DWORD
	v_and_b32_sdwa v22, v19, v55 dst_sel:DWORD dst_unused:UNUSED_PAD src0_sel:WORD_1 src1_sel:DWORD
	v_and_b32_sdwa v23, v18, v55 dst_sel:DWORD dst_unused:UNUSED_PAD src0_sel:WORD_1 src1_sel:DWORD
	v_add3_u32 v21, v21, v24, s9
	v_add3_u32 v20, v20, v25, s9
	v_add3_u32 v18, v18, v23, s9
	v_add3_u32 v19, v19, v22, s9
	v_and_b32_e32 v21, 0xffff0000, v21
	v_and_b32_e32 v20, 0xffff0000, v20
	v_or_b32_sdwa v19, v21, v19 dst_sel:DWORD dst_unused:UNUSED_PAD src0_sel:DWORD src1_sel:WORD_1
	v_or_b32_sdwa v18, v20, v18 dst_sel:DWORD dst_unused:UNUSED_PAD src0_sel:DWORD src1_sel:WORD_1
	global_store_dwordx2 v[46:47], v[18:19], off offset:1536
	global_load_dwordx4 v[18:21], v[36:37], off
	v_mov_b32_e32 v22, v14
	v_mov_b32_e32 v23, v16
	v_mov_b32_e32 v16, v15
	v_pk_mul_f32 v[14:15], v[22:23], v[26:27] op_sel_hi:[1,0]
	v_pk_mul_f32 v[16:17], v[16:17], v[26:27] op_sel_hi:[1,0]
	s_waitcnt vmcnt(0)
	v_mov_b32_e32 v23, v20
	v_mov_b32_e32 v20, v19
	v_mov_b32_e32 v22, v18
	v_pk_mul_f32 v[16:17], v[16:17], v[20:21]
	v_pk_mul_f32 v[14:15], v[14:15], v[22:23]
	v_and_b32_sdwa v20, v17, v55 dst_sel:DWORD dst_unused:UNUSED_PAD src0_sel:WORD_1 src1_sel:DWORD
	v_and_b32_sdwa v21, v16, v55 dst_sel:DWORD dst_unused:UNUSED_PAD src0_sel:WORD_1 src1_sel:DWORD
	v_and_b32_sdwa v18, v15, v55 dst_sel:DWORD dst_unused:UNUSED_PAD src0_sel:WORD_1 src1_sel:DWORD
	v_and_b32_sdwa v19, v14, v55 dst_sel:DWORD dst_unused:UNUSED_PAD src0_sel:WORD_1 src1_sel:DWORD
	v_add3_u32 v17, v17, v20, s9
	v_add3_u32 v16, v16, v21, s9
	v_add3_u32 v14, v14, v19, s9
	v_add3_u32 v15, v15, v18, s9
	v_and_b32_e32 v17, 0xffff0000, v17
	v_and_b32_e32 v16, 0xffff0000, v16
	v_or_b32_sdwa v15, v17, v15 dst_sel:DWORD dst_unused:UNUSED_PAD src0_sel:DWORD src1_sel:WORD_1
	v_or_b32_sdwa v14, v16, v14 dst_sel:DWORD dst_unused:UNUSED_PAD src0_sel:DWORD src1_sel:WORD_1
	global_store_dwordx2 v[46:47], v[14:15], off offset:2048
	global_load_dwordx4 v[14:17], v[38:39], off
	v_mov_b32_e32 v18, v10
	v_mov_b32_e32 v19, v12
	v_mov_b32_e32 v12, v11
	v_pk_mul_f32 v[10:11], v[18:19], v[26:27] op_sel_hi:[1,0]
	v_pk_mul_f32 v[12:13], v[12:13], v[26:27] op_sel_hi:[1,0]
	s_waitcnt vmcnt(0)
	v_mov_b32_e32 v19, v16
	v_mov_b32_e32 v16, v15
	v_mov_b32_e32 v18, v14
	v_pk_mul_f32 v[12:13], v[12:13], v[16:17]
	v_pk_mul_f32 v[10:11], v[10:11], v[18:19]
	v_and_b32_sdwa v16, v13, v55 dst_sel:DWORD dst_unused:UNUSED_PAD src0_sel:WORD_1 src1_sel:DWORD
	v_and_b32_sdwa v17, v12, v55 dst_sel:DWORD dst_unused:UNUSED_PAD src0_sel:WORD_1 src1_sel:DWORD
	v_and_b32_sdwa v14, v11, v55 dst_sel:DWORD dst_unused:UNUSED_PAD src0_sel:WORD_1 src1_sel:DWORD
	v_and_b32_sdwa v15, v10, v55 dst_sel:DWORD dst_unused:UNUSED_PAD src0_sel:WORD_1 src1_sel:DWORD
	v_add3_u32 v13, v13, v16, s9
	v_add3_u32 v12, v12, v17, s9
	v_add3_u32 v10, v10, v15, s9
	v_add3_u32 v11, v11, v14, s9
	v_and_b32_e32 v13, 0xffff0000, v13
	v_and_b32_e32 v12, 0xffff0000, v12
	v_or_b32_sdwa v11, v13, v11 dst_sel:DWORD dst_unused:UNUSED_PAD src0_sel:DWORD src1_sel:WORD_1
	v_or_b32_sdwa v10, v12, v10 dst_sel:DWORD dst_unused:UNUSED_PAD src0_sel:DWORD src1_sel:WORD_1
	global_store_dwordx2 v[46:47], v[10:11], off offset:2560
	global_load_dwordx4 v[10:13], v[40:41], off
	v_mov_b32_e32 v14, v6
	v_mov_b32_e32 v15, v8
	v_mov_b32_e32 v8, v7
	v_pk_mul_f32 v[6:7], v[14:15], v[26:27] op_sel_hi:[1,0]
	v_pk_mul_f32 v[8:9], v[8:9], v[26:27] op_sel_hi:[1,0]
	s_waitcnt vmcnt(0)
	v_mov_b32_e32 v15, v12
	v_mov_b32_e32 v12, v11
	v_mov_b32_e32 v14, v10
	v_pk_mul_f32 v[8:9], v[8:9], v[12:13]
	v_pk_mul_f32 v[6:7], v[6:7], v[14:15]
	v_and_b32_sdwa v12, v9, v55 dst_sel:DWORD dst_unused:UNUSED_PAD src0_sel:WORD_1 src1_sel:DWORD
	v_and_b32_sdwa v13, v8, v55 dst_sel:DWORD dst_unused:UNUSED_PAD src0_sel:WORD_1 src1_sel:DWORD
	v_and_b32_sdwa v10, v7, v55 dst_sel:DWORD dst_unused:UNUSED_PAD src0_sel:WORD_1 src1_sel:DWORD
	v_and_b32_sdwa v11, v6, v55 dst_sel:DWORD dst_unused:UNUSED_PAD src0_sel:WORD_1 src1_sel:DWORD
	v_add3_u32 v9, v9, v12, s9
	v_add3_u32 v8, v8, v13, s9
	v_add3_u32 v6, v6, v11, s9
	v_add3_u32 v7, v7, v10, s9
	v_and_b32_e32 v9, 0xffff0000, v9
	v_and_b32_e32 v8, 0xffff0000, v8
	v_or_b32_sdwa v7, v9, v7 dst_sel:DWORD dst_unused:UNUSED_PAD src0_sel:DWORD src1_sel:WORD_1
	v_or_b32_sdwa v6, v8, v6 dst_sel:DWORD dst_unused:UNUSED_PAD src0_sel:DWORD src1_sel:WORD_1
	global_store_dwordx2 v[46:47], v[6:7], off offset:3072
	global_load_dwordx4 v[6:9], v[42:43], off
	v_mov_b32_e32 v10, v2
	v_mov_b32_e32 v11, v4
	v_mov_b32_e32 v4, v3
	v_pk_mul_f32 v[2:3], v[10:11], v[26:27] op_sel_hi:[1,0]
	v_pk_mul_f32 v[4:5], v[4:5], v[26:27] op_sel_hi:[1,0]
	s_waitcnt vmcnt(0)
	v_mov_b32_e32 v11, v8
	v_mov_b32_e32 v8, v7
	v_mov_b32_e32 v10, v6
	v_pk_mul_f32 v[4:5], v[4:5], v[8:9]
	v_pk_mul_f32 v[2:3], v[2:3], v[10:11]
	v_and_b32_sdwa v8, v5, v55 dst_sel:DWORD dst_unused:UNUSED_PAD src0_sel:WORD_1 src1_sel:DWORD
	v_and_b32_sdwa v9, v4, v55 dst_sel:DWORD dst_unused:UNUSED_PAD src0_sel:WORD_1 src1_sel:DWORD
	v_and_b32_sdwa v6, v3, v55 dst_sel:DWORD dst_unused:UNUSED_PAD src0_sel:WORD_1 src1_sel:DWORD
	v_and_b32_sdwa v7, v2, v55 dst_sel:DWORD dst_unused:UNUSED_PAD src0_sel:WORD_1 src1_sel:DWORD
	v_add3_u32 v5, v5, v8, s9
	v_add3_u32 v4, v4, v9, s9
	v_add3_u32 v2, v2, v7, s9
	v_add3_u32 v3, v3, v6, s9
	v_and_b32_e32 v5, 0xffff0000, v5
	v_and_b32_e32 v4, 0xffff0000, v4
	v_or_b32_sdwa v3, v5, v3 dst_sel:DWORD dst_unused:UNUSED_PAD src0_sel:DWORD src1_sel:WORD_1
	v_or_b32_sdwa v2, v4, v2 dst_sel:DWORD dst_unused:UNUSED_PAD src0_sel:DWORD src1_sel:WORD_1
	global_store_dwordx2 v[46:47], v[2:3], off offset:3584
	v_lshl_add_u64 v[46:47], v[46:47], 0, s[12:13]
	s_cbranch_scc1 .LBB0_25
